# attention K staging: each LDS-DMA piece covers 8 key rows x 128B (swizzled [key][chunk] LDS layout) instead of 64 rows x 16B
# speedup vs baseline: 1.0063x; 1.0063x over previous
; #define GAS __attribute__((address_space(1)))
; #define LAS __attribute__((address_space(3)))
; #define WG_BAR() do { asm volatile("s_waitcnt vmcnt(0) lgkmcnt(0)" ::: "memory"); __builtin_amdgcn_s_barrier(); asm volatile("" ::: "memory"); } while (0)
; __device__ __forceinline__ int swap23(int i) { return (i & 0x13) | ((i & 4) << 1) | ((i & 8) >> 1); }
; __device__ __forceinline__ unsigned tr_off(int lane, int c, int t) { const int h = lane >> 5, blk = (lane >> 4) & 1, q = (lane & 15) >> 2, p = lane & 3; return offb(8 * h + 4 * t + q, 4 * c + 2 * blk + (p >> 1)) + 8u * (unsigned)(p & 1); }
; __device__ __forceinline__ void attn_unit(LAS unsigned char* lds, const bf16* proj, bf16* Y, const float* relb, const float* hgain, float lam, float oscale, int b, int h, int qb, int tid, int lane, int wid, Stopwatch& sw) {
;     ...
;     const int r32 = lane & 31, hi = lane >> 5, mp = wid >> 2, wq = wid & 3;
;     const int q0 = qb * 128, qw = q0 + 32 * wq;
;     const size_t rowbase = (size_t)b * SEQ;
;     LAS float* tab = (LAS float*)(lds + 98304);
;     if (tid < 129) tab[tid] = relb[t5_bucket(tid) * 8 + h] * LOG2E;
;     const float bias31 = relb[31 * 8 + h] * LOG2E;
;     LAS unsigned char* qlds = lds + 100352 + wid * 4096 + hi * 512 + r32 * 16;
;     { const bf16* qp = proj + (rowbase + qw + r32) * LDP + C_QD + h * 128 + mp * 64 + hi * 8;
; #pragma unroll
;       for (int d0 = 0; d0 < 4; ++d0) *(LAS bf16x8*)(qlds + d0 * 1024) = *(const GAS bf16x8*)(qp + d0 * 16); }
;     const bf16* k0src = proj + (rowbase + (lane & 32) + swap23(r32)) * LDP + C_KD + h * 128 + wid * 8;
;     const bf16* k1src = k0src + 64;
;     const bf16* vsrc[2];
; #pragma unroll
;     for (int i = 0; i < 2; ++i) { const int vrow = 8 * wid + 4 * i + (lane >> 4); const int ch = (lane & 15) ^ (((vrow & 3) << 2) | ((vrow >> 2) & 3)); vsrc[i] = proj + (rowbase + vrow) * LDP + C_VD + h * 128 + ch * 8; }
;     ...
;     unsigned va[4][2];
; #pragma unroll
;     for (int c = 0; c < 4; ++c) { va[c][0] = 16384u + tr_off(lane, c, 0); va[c][1] = 16384u + tr_off(lane, c, 1); }
;     const unsigned kboff = mp * 8192 + hi * 1024 + r32 * 16;
;     const int NT = 2 * qb + 2;
;     ATT_DMA(0, lds); ATT_DMA(1, lds + 32768);
;     float m_run = -1e30f, l_run = 0.f;
;     f32x16 o[4];
; #pragma unroll
;     for (int c = 0; c < 4; ++c) o[c] = splat16(0.f);
;     const int qi = qw + r32;
;     ...
;     WG_BAR();
.LBB0_360:
	s_or_b64 exec, exec, s[36:37]
	s_ashr_i32 s24, s3, 6
	s_lshl_b32 s5, s19, 7
	v_readlane_b32 s3, v252, 60
	v_and_b32_e32 v60, 31, v61
	s_or_b32 s16, s5, s3
	s_ashr_i32 s25, s24, 31
	s_lshl_b64 s[36:37], s[24:25], 12
	v_or_b32_e32 v64, s16, v60
	v_or_b32_e32 v151, s36, v64
	v_mov_b64_e32 v[20:21], s[12:13]
	v_mad_u64_u32 v[4:5], s[24:25], v151, s33, v[20:21]
	s_lshl_b32 s3, s0, 2
	v_readlane_b32 s40, v250, 2
	v_mad_i32_i24 v5, s37, v239, v5
	s_lshl_b32 s34, s0, 8
	v_bfe_u32 v44, v61, 5, 1
	v_mov_b32_e32 v2, s3
	v_readlane_b32 s42, v250, 4
	v_readlane_b32 s43, v250, 5
	v_lshl_add_u64 v[4:5], v[4:5], 0, s[34:35]
	s_lshl_b32 s24, s31, 1
	s_mov_b32 s25, s35
	v_lshl_add_u64 v[4:5], v[4:5], 0, s[24:25]
	s_movk_i32 s3, 0x3000
	global_load_dword v34, v2, s[42:43] offset:992
	v_lshlrev_b32_e32 v2, 4, v44
	v_lshl_add_u64 v[4:5], v[4:5], 0, v[2:3]
	s_mov_b64 s[24:25], 0x3800
	v_add_co_u32_e32 v16, vcc, s3, v4
	v_lshl_add_u64 v[12:13], v[4:5], 0, s[24:25]
	s_nop 0
	v_addc_co_u32_e32 v17, vcc, 0, v5, vcc
	global_load_dwordx4 v[4:7], v[12:13], off offset:32
	global_load_dwordx4 v[8:11], v[12:13], off offset:64
	s_nop 0
	global_load_dwordx4 v[12:15], v[12:13], off offset:96
	s_nop 0
	global_load_dwordx4 v[16:19], v[16:17], off offset:2048
	v_bfe_u32 v26, v61, 4, 2
	v_readlane_b32 s3, v252, 58
	v_lshlrev_b32_e32 v22, 1, v61
	v_lshrrev_b32_e32 v63, 1, v61
	v_and_b32_e32 v24, 51, v61
	v_readlane_b32 s18, v252, 61
	v_and_b32_e32 v28, 15, v61
	v_lshl_add_u32 v30, v44, 9, s3
	v_lshlrev_b32_e32 v31, 4, v60
	v_lshlrev_b32_e32 v35, 2, v26
	v_readlane_b32 s3, v252, 59
	v_and_b32_e32 v32, 8, v22
	v_and_or_b32 v24, v63, 4, v24
	v_or_b32_e32 v22, s18, v26
	v_lshlrev_b32_e32 v33, 10, v44
	v_add_u32_e32 v62, v30, v31
	v_bitop3_b32 v30, v35, v28, s3 bitop3:0x36
	v_readlane_b32 s3, v252, 62
	v_mov_b32_e32 v23, v3
	v_mov_b32_e32 v27, v3
	v_or_b32_e32 v26, 4, v22
	v_lshrrev_b32_e32 v164, 1, v60
	v_xor_b32_e32 v164, v164, v44
	v_and_b32_e32 v164, 1, v164
	v_lshlrev_b32_e32 v164, 4, v164
	v_bfe_u32 v206, v60, 2, 2
	v_lshl_or_b32 v164, v206, 5, v164
	v_lshl_or_b32 v164, v60, 7, v164
	v_or_b32_e32 v164, s3, v164
	v_or3_b32 v31, v24, v32, s36
	v_lshl_add_u64 v[22:23], s[36:37], 0, v[22:23]
	v_lshlrev_b32_e32 v24, 4, v30
	v_bfe_u32 v36, v26, 2, 2
	v_lshl_add_u64 v[26:27], s[36:37], 0, v[26:27]
	v_mad_u64_u32 v[30:31], s[24:25], v31, s33, v[20:21]
	v_mad_u64_u32 v[32:33], s[24:25], v22, s33, v[20:21]
	v_bitop3_b32 v22, v36, v28, v35 bitop3:0x36
	v_mad_u64_u32 v[20:21], s[24:25], v26, s33, v[20:21]
	v_mad_i32_i24 v31, s37, v239, v31
	s_lshl_b32 s38, s18, 1
	s_mov_b32 s39, s35
	v_mad_i32_i24 v33, v23, s33, v33
	v_mad_i32_i24 v21, v27, s33, v21
	v_lshlrev_b32_e32 v28, 4, v22
	v_lshl_add_u64 v[22:23], v[30:31], 0, s[34:35]
	v_mov_b32_e32 v25, v3
	v_mov_b32_e32 v29, v3
	v_lshl_add_u64 v[26:27], v[32:33], 0, s[34:35]
	v_lshl_add_u64 v[20:21], v[20:21], 0, s[34:35]
	v_lshl_add_u64 v[22:23], v[22:23], 0, s[38:39]
	v_and_b32_e32 v206, 63, v61
	v_lshrrev_b32_e32 v207, 3, v206
	v_add_u32_e32 v207, s18, v207
	v_and_b32_e32 v208, 0x33, v207
	v_lshlrev_b32_e32 v209, 1, v207
	v_and_b32_e32 v209, 8, v209
	v_or_b32_e32 v208, v208, v209
	v_lshrrev_b32_e32 v209, 1, v207
	v_and_b32_e32 v209, 4, v209
	v_or_b32_e32 v208, v208, v209
	v_add_u32_e32 v208, s36, v208
	v_lshrrev_b32_e32 v209, 1, v207
	v_and_b32_e32 v209, 7, v209
	v_and_b32_e32 v206, 7, v206
	v_xor_b32_e32 v206, v206, v209
	v_lshlrev_b32_e32 v206, 4, v206
	v_add_u32_e32 v206, s34, v206
	v_mov_b32_e32 v207, 0
	v_lshl_add_u64 v[206:207], s[12:13], 0, v[206:207]
	v_mad_u64_u32 v[22:23], s[100:101], v208, s33, v[206:207]
	s_mov_b64 s[24:25], 0x4000
	v_lshl_add_u64 v[24:25], v[26:27], 0, v[24:25]
	v_lshl_add_u64 v[20:21], v[20:21], 0, v[28:29]
	v_lshl_add_u64 v[52:53], v[22:23], 0, s[24:25]
	s_mov_b64 s[24:25], 0x4800
	v_lshl_add_u64 v[54:55], v[24:25], 0, s[24:25]
	v_lshl_add_u64 v[58:59], v[20:21], 0, s[24:25]
	s_mov_b64 s[24:25], 0x4080
	v_readlane_b32 s18, v253, 3
	v_lshl_add_u64 v[56:57], v[22:23], 0, s[24:25]
	s_waitcnt vmcnt(3)
	ds_write_b128 v62, v[4:7] offset:1024
	s_waitcnt vmcnt(2)
	ds_write_b128 v62, v[8:11] offset:2048
	s_waitcnt vmcnt(1)
	ds_write_b128 v62, v[12:15] offset:3072
	s_waitcnt vmcnt(0)
	ds_write_b128 v62, v[16:19]
	s_mov_b32 s3, m0
	s_mov_b32 m0, s18
	s_nop 0
	global_load_lds_dwordx4 v[52:53], off
	s_mov_b32 m0, s3
	v_readlane_b32 s18, v252, 63
	s_mov_b32 s3, m0
	s_mov_b32 m0, s18
	s_nop 0
	global_load_lds_dwordx4 v[56:57], off
	s_mov_b32 m0, s3
	v_readlane_b32 s18, v253, 0
	s_mov_b32 s3, m0
	s_mov_b32 m0, s18
	s_nop 0
	global_load_lds_dwordx4 v[54:55], off
	s_mov_b32 m0, s3
	s_mov_b64 s[24:25], 0x1c4000
	v_readlane_b32 s18, v253, 1
	s_mov_b32 s3, m0
	s_mov_b32 m0, s18
	s_nop 0
	global_load_lds_dwordx4 v[58:59], off
	s_mov_b32 m0, s3
	v_lshl_add_u64 v[26:27], v[22:23], 0, s[24:25]
	s_mov_b64 s[24:25], 0x1c4080
	v_readlane_b32 s18, v253, 2
	s_mov_b32 s3, m0
	s_mov_b32 m0, s18
	s_nop 0
	global_load_lds_dwordx4 v[26:27], off
	s_mov_b32 m0, s3
	v_lshl_add_u64 v[22:23], v[22:23], 0, s[24:25]
	s_mov_b64 s[24:25], 0x1c4800
	v_readlane_b32 s18, v253, 4
	s_mov_b32 s3, m0
	s_mov_b32 m0, s18
	s_nop 0
	global_load_lds_dwordx4 v[22:23], off
	s_mov_b32 m0, s3
	v_lshl_add_u64 v[24:25], v[24:25], 0, s[24:25]
	v_readlane_b32 s18, v253, 5
	s_mov_b32 s3, m0
	s_mov_b32 m0, s18
	s_nop 0
	global_load_lds_dwordx4 v[24:25], off
	s_mov_b32 m0, s3
	v_lshl_add_u64 v[20:21], v[20:21], 0, s[24:25]
	v_readlane_b32 s18, v253, 6
	s_mov_b32 s3, m0
	s_mov_b32 m0, s18
	s_nop 0
	global_load_lds_dwordx4 v[20:21], off
	s_mov_b32 m0, s3
	v_mul_f32_e32 v204, 0x3fb8aa3b, v34
	v_cmp_gt_u32_e32 vcc, 0x60, v61
	v_add_u32_e32 v205, 0x81, v61
	s_nop 0
	v_cndmask_b32_e32 v204, v204, v246, vcc
	v_cndmask_b32_e32 v205, v205, v61, vcc
	v_lshlrev_b32_e32 v205, 2, v205
	v_add_u32_e32 v205, 0x20800, v205
	v_cmp_gt_u32_e32 vcc, 0xbf, v61
	s_and_saveexec_b64 s[100:101], vcc
	ds_write_b32 v205, v204
	s_or_b64 exec, exec, s[100:101]
	s_waitcnt vmcnt(0) lgkmcnt(0)
	s_barrier
; #define TS_END(sw, id) do { if ((id) == TSSEL && (sw).on) (sw).acc += __builtin_amdgcn_s_memrealtime() - (sw).t0; } while (0)
; #define TS_END(sw, id) do { } while (0)
; #define WG_BAR() do { asm volatile("s_waitcnt vmcnt(0) lgkmcnt(0)" ::: "memory"); __builtin_amdgcn_s_barrier(); asm volatile("" ::: "memory"); } while (0)
; #define ATT_QK(S0, S1, sbp, cin) do { S0 = splat16(cin); S1 = S0; \
;         _Pragma("unroll") for (int d0 = 0; d0 < 4; ++d0) { const bf16x8 kf0_ = *(const LAS bf16x8*)((sbp) + kboff + d0 * 2048), kf1_ = *(const LAS bf16x8*)((sbp) + kboff + d0 * 2048 + 512), q_ = *(const LAS bf16x8*)(qlds + d0 * 1024); \
;             S0 = MFMA32(kf0_, q_, S0); S1 = MFMA32(kf1_, q_, S1); } } while (0)
; __device__ __forceinline__ void attn_unit(LAS unsigned char* lds, const bf16* proj, bf16* Y, const float* relb, const float* hgain, float lam, float oscale, int b, int h, int qb, int tid, int lane, int wid, Stopwatch& sw) {
;     ...
;     WG_BAR();
;     TS_END(sw, 8);
;     f32x16 sA0, sA1, sB0, sB1;
;     typedef __bf16 bf2_t_ __attribute__((ext_vector_type(2)));
;     const bf2_t_ one2 = __builtin_bit_cast(bf2_t_, 0x3F803F80u);
;     { const bool far0 = (63 + 128 <= qw); ATT_QK(sA0, sA1, lds, far0 ? bias31 : 0.f);
;       if (!far0) {
; #pragma unroll
;           for (int r = 0; r < 16; ++r) { const int key = 16 * (r >> 3) + 8 * hi + (r & 7); const int d0_ = qi - key, d1_ = d0_ - 32;
;               const float b0 = tab[d0_ < 0 ? 0 : (d0_ > 128 ? 128 : d0_)], b1 = tab[d1_ < 0 ? 0 : (d1_ > 128 ? 128 : d1_)];
;               sA0[r] = d0_ < 0 ? -1e30f : sA0[r] + b0; sA1[r] = d1_ < 0 ? -1e30f : sA1[r] + b1; } }
	v_add_u32_e32 v45, 0, v164
	v_xor_b32_e32 v206, 32, v45
	v_xor_b32_e32 v207, 64, v45
	v_xor_b32_e32 v208, 0x60, v45
	ds_read_b128 v[36:39], v45
	ds_read_b128 v[40:43], v62
	s_cmpk_gt_u32 s16, 0xbe
	v_mul_f32_e32 v165, 0x3fb8aa3b, v34
	s_cselect_b64 vcc, -1, 0
	v_cndmask_b32_e32 v4, 0, v165, vcc
	v_mov_b32_e32 v5, v4
	v_mov_b32_e32 v6, v4
	v_mov_b32_e32 v7, v4
	v_mov_b32_e32 v8, v4
	v_mov_b32_e32 v9, v4
	v_mov_b32_e32 v10, v4
	v_mov_b32_e32 v11, v4
	v_mov_b32_e32 v12, v4
	v_mov_b32_e32 v13, v4
	v_mov_b32_e32 v14, v4
	v_mov_b32_e32 v15, v4
	v_mov_b32_e32 v16, v4
	v_mov_b32_e32 v17, v4
	v_mov_b32_e32 v18, v4
	v_mov_b32_e32 v19, v4
	v_mov_b32_e32 v163, s37
	v_lshlrev_b32_e32 v150, 3, v44
	s_waitcnt lgkmcnt(0)
	v_mfma_f32_32x32x16_bf16 v[20:35], v[36:39], v[40:43], v[4:19]
	ds_read_b128 v[36:39], v45 offset:4096
	s_and_b64 vcc, exec, vcc
	v_readlane_b32 s41, v250, 3
	v_readlane_b32 s44, v250, 6
	v_readlane_b32 s45, v250, 7
	v_readlane_b32 s46, v250, 8
	v_readlane_b32 s47, v250, 9
	s_waitcnt lgkmcnt(0)
	v_mfma_f32_32x32x16_bf16 v[4:19], v[36:39], v[40:43], v[4:19]
	ds_read_b128 v[36:39], v206
	ds_read_b128 v[40:43], v62 offset:1024
	v_readlane_b32 s48, v250, 10
	v_readlane_b32 s49, v250, 11
	v_readlane_b32 s50, v250, 12
	v_readlane_b32 s51, v250, 13
	v_readlane_b32 s52, v250, 14
	v_readlane_b32 s53, v250, 15
	s_waitcnt lgkmcnt(0)
	v_mfma_f32_32x32x16_bf16 v[20:35], v[36:39], v[40:43], v[20:35]
	ds_read_b128 v[36:39], v206 offset:4096
	v_readlane_b32 s54, v250, 16
	v_readlane_b32 s55, v250, 17
	s_waitcnt lgkmcnt(0)
	v_mfma_f32_32x32x16_bf16 v[4:19], v[36:39], v[40:43], v[4:19]
	ds_read_b128 v[36:39], v207
	ds_read_b128 v[40:43], v62 offset:2048
	s_waitcnt lgkmcnt(0)
	v_mfma_f32_32x32x16_bf16 v[20:35], v[36:39], v[40:43], v[20:35]
	ds_read_b128 v[36:39], v207 offset:4096
	s_waitcnt lgkmcnt(0)
	v_mfma_f32_32x32x16_bf16 v[4:19], v[36:39], v[40:43], v[4:19]
	ds_read_b128 v[36:39], v208
	ds_read_b128 v[40:43], v62 offset:3072
	s_waitcnt lgkmcnt(0)
	v_mfma_f32_32x32x16_bf16 v[20:35], v[36:39], v[40:43], v[20:35]
	ds_read_b128 v[36:39], v208 offset:4096
	s_waitcnt lgkmcnt(0)
	v_mfma_f32_32x32x16_bf16 v[4:19], v[36:39], v[40:43], v[4:19]
	s_cbranch_vccnz .LBB0_394
	v_sub_u32_e32 v38, v64, v150
	v_min_i32_e32 v36, 0xa0, v38
	v_subrev_u32_e32 v36, 32, v36
	v_cmp_gt_i32_e32 vcc, 32, v38
	v_cmp_lt_i32_e64 s[36:37], -1, v38
	v_mov_b32_e32 v37, 0xf149f2ca
	v_cndmask_b32_e64 v36, v36, 0, vcc
	v_lshl_add_u32 v36, v36, 2, 0
	v_add_u32_e32 v36, 0x18000, v36
	ds_read_b32 v65, v36
	v_mov_b32_e32 v36, 0xf149f2ca
	s_and_saveexec_b64 s[38:39], s[36:37]
	s_cbranch_execz .LBB0_363
	v_min_u32_e32 v36, 0x80, v38
	v_lshl_add_u32 v36, v36, 2, 0
	v_add_u32_e32 v36, 0x18000, v36
	ds_read_b32 v36, v36
	s_waitcnt lgkmcnt(0)
	v_add_f32_e32 v36, v20, v36

.LBB0_397:
	s_add_i32 s0, s34, 0x80
	s_cmp_le_u32 s0, s24
	s_cselect_b64 s[78:79], -1, 0
	s_add_i32 s82, s31, 0
	s_add_i32 s3, s34, 0x13f
	s_cmp_gt_u32 s3, s16
	s_cselect_b64 s[36:37], -1, 0
	s_cmp_gt_u32 s0, s24
	s_cbranch_scc1 .Latt_noqk
	v_add_u32_e32 v152, s82, v164
	v_xor_b32_e32 v220, 32, v152
	v_xor_b32_e32 v221, 64, v152
	v_xor_b32_e32 v222, 0x60, v152
	ds_read_b128 v[204:207], v152
	ds_read_b128 v[208:211], v152 offset:4096
	ds_read_b128 v[212:215], v220
	ds_read_b128 v[216:219], v220 offset:4096
	s_add_i32 s0, s73, 0
	v_add_u32_e32 v196, s0, v171
	v_add_u32_e32 v197, s0, v170
	v_add_u32_e32 v202, s0, v169
	v_add_u32_e32 v203, s0, v168
	ds_read_b64_tr_b16 v[178:179], v196 offset:16384
	ds_read_b64_tr_b16 v[180:181], v197 offset:16384
	ds_read_b64_tr_b16 v[184:185], v197 offset:20480
	ds_read_b64_tr_b16 v[182:183], v196 offset:20480
	ds_read_b64_tr_b16 v[186:187], v202 offset:16384
	ds_read_b64_tr_b16 v[188:189], v203 offset:16384
	ds_read_b64_tr_b16 v[192:193], v203 offset:20480
	ds_read_b64_tr_b16 v[190:191], v202 offset:20480
	v_cndmask_b32_e64 v68, v165, 0, s[36:37]
	v_sub_f32_e32 v68, v68, v167
	v_mov_b32_e32 v82, v68
	v_mov_b32_e32 v83, v68
	v_mov_b32_e32 v69, v68
	v_mov_b32_e32 v70, v68
	v_mov_b32_e32 v71, v68
	v_mov_b32_e32 v72, v68
	v_mov_b32_e32 v73, v68
	v_mov_b32_e32 v74, v68
	v_mov_b32_e32 v75, v68
	v_mov_b32_e32 v76, v68
	v_mov_b32_e32 v77, v68
	v_mov_b32_e32 v78, v68
	v_mov_b32_e32 v79, v68
	v_mov_b32_e32 v80, v68
	v_mov_b32_e32 v81, v68
	s_nop 1
	s_waitcnt lgkmcnt(11)
	v_mfma_f32_32x32x16_bf16 v[100:115], v[204:207], v[116:119], v[68:83]
	s_waitcnt lgkmcnt(10)
	v_mfma_f32_32x32x16_bf16 v[84:99], v[208:211], v[116:119], v[68:83]
	s_waitcnt lgkmcnt(9)
	v_mfma_f32_32x32x16_bf16 v[100:115], v[212:215], v[120:123], v[100:115]
	ds_read_b128 v[204:207], v221
	ds_read_b128 v[208:211], v221 offset:4096
	ds_read_b128 v[212:215], v222
	s_waitcnt lgkmcnt(11)
	v_mfma_f32_32x32x16_bf16 v[84:99], v[216:219], v[120:123], v[84:99]
	ds_read_b128 v[216:219], v222 offset:4096
	s_waitcnt lgkmcnt(3)
	v_mfma_f32_32x32x16_bf16 v[100:115], v[204:207], v[124:127], v[100:115]
	s_waitcnt lgkmcnt(2)
	v_mfma_f32_32x32x16_bf16 v[84:99], v[208:211], v[124:127], v[84:99]
	s_waitcnt lgkmcnt(1)
	v_mfma_f32_32x32x16_bf16 v[68:83], v[212:215], v[128:131], v[100:115]
	s_waitcnt lgkmcnt(0)
	v_mfma_f32_32x32x16_bf16 v[84:99], v[216:219], v[128:131], v[84:99]
	s_andn2_b64 vcc, exec, s[36:37]
	s_cbranch_vccnz .LBB0_432
	v_add_u32_e32 v177, s5, v176
	s_mov_b32 s100, 0x207a4
	v_lshl_add_u32 v177, v177, 2, s100
	ds_read2_b32 v[204:205], v177 offset0:55 offset1:54
	ds_read2_b32 v[206:207], v177 offset0:53 offset1:52
	ds_read2_b32 v[208:209], v177 offset0:51 offset1:50
	ds_read2_b32 v[210:211], v177 offset0:49 offset1:48
	ds_read2_b32 v[212:213], v177 offset0:39 offset1:38
	ds_read2_b32 v[214:215], v177 offset0:37 offset1:36
	ds_read2_b32 v[216:217], v177 offset0:35 offset1:34
	ds_read2_b32 v[218:219], v177 offset0:33 offset1:32
	ds_read2_b32 v[220:221], v177 offset0:23 offset1:22
	ds_read2_b32 v[222:223], v177 offset0:21 offset1:20
	ds_read2_b32 v[224:225], v177 offset0:19 offset1:18
	ds_read2_b32 v[226:227], v177 offset0:17 offset1:16
	ds_read2_b32 v[228:229], v177 offset0:7 offset1:6
	ds_read2_b32 v[230:231], v177 offset0:5 offset1:4
	ds_read2_b32 v[232:233], v177 offset0:3 offset1:2
	s_waitcnt lgkmcnt(14)
	v_pk_add_f32 v[68:69], v[68:69], v[204:205]
	ds_read2_b32 v[204:205], v177 offset0:1 offset1:0
	s_waitcnt lgkmcnt(8)
	v_pk_add_f32 v[70:71], v[70:71], v[206:207]
	v_pk_add_f32 v[72:73], v[72:73], v[208:209]
	v_pk_add_f32 v[74:75], v[74:75], v[210:211]
	v_pk_add_f32 v[76:77], v[76:77], v[212:213]
	v_pk_add_f32 v[78:79], v[78:79], v[214:215]
	v_pk_add_f32 v[80:81], v[80:81], v[216:217]
	v_pk_add_f32 v[82:83], v[82:83], v[218:219]
	s_waitcnt lgkmcnt(0)
	v_pk_add_f32 v[84:85], v[84:85], v[220:221]
	v_pk_add_f32 v[86:87], v[86:87], v[222:223]
	v_pk_add_f32 v[88:89], v[88:89], v[224:225]
	v_pk_add_f32 v[90:91], v[90:91], v[226:227]
	v_pk_add_f32 v[92:93], v[92:93], v[228:229]
	v_pk_add_f32 v[94:95], v[94:95], v[230:231]
	v_pk_add_f32 v[96:97], v[96:97], v[232:233]
	v_pk_add_f32 v[98:99], v[98:99], v[204:205]
